# MoE down-GEMM scatter epilogue de-serialised only; unreachable padding keeps every other instruction at its baseline address
# speedup vs baseline: 1.0128x; 1.0128x over previous
.LBB0_1086:
	s_or_b64 exec, exec, s[36:37]
	s_andn2_b64 vcc, exec, s[30:31]
	s_mov_b64 s[30:31], -1
	s_cbranch_vccnz .LBB0_1065
	s_andn2_b64 vcc, exec, s[4:5]
	s_cbranch_vccnz .LBB0_1064
	s_barrier
	s_branch .LBB0_1064
	s_nop 0
	s_nop 0
	s_nop 0
	s_nop 0
	s_nop 0
	s_nop 0
	s_nop 0
	s_nop 0
	s_nop 0
	s_nop 0
	s_nop 0
	s_nop 0
	s_nop 0
	s_nop 0
	s_nop 0
	s_nop 0
	s_nop 0
	s_nop 0
	s_nop 0
	s_nop 0
	s_nop 0
	s_nop 0
	s_nop 0
	s_nop 0
	s_nop 0
	s_nop 0
	s_nop 0
	s_nop 0
	s_nop 0
	s_nop 0
	s_nop 0
	s_nop 0
	s_nop 0
	s_nop 0
	s_nop 0
	s_nop 0
	s_nop 0
	s_nop 0
	s_nop 0
	s_nop 0
	s_nop 0
	s_nop 0
	s_nop 0
	s_nop 0
	s_nop 0
	s_nop 0
	s_nop 0
	s_nop 0
	s_nop 0
	s_nop 0
	s_nop 0
	s_nop 0
	s_nop 0
	s_nop 0
	s_nop 0
	s_nop 0
	s_nop 0
	s_nop 0
	s_nop 0
	s_nop 0
	s_nop 0
	s_nop 0
	s_nop 0
	s_nop 0
	s_nop 0
	s_nop 0
	s_nop 0
	s_nop 0
	s_nop 0
	s_nop 0
	s_nop 0
